# P6: next unit's gathered-row list entries kept in VGPRs (no LDS slot round trip, no vmcnt(0) at unit top), first-iteration second wait leaves them in flight
# baseline (speedup 1.0000x reference)
;     __device__ __forceinline__ bool next(int i, Unit& u) const {
;         int v = c;
;         if ((G & 7) == 0) { const int rem = nunits - i * G;
;             if (rem >= G) v = (c & 7) * (G >> 3) + (c >> 3);
;             else { const int per = (rem + 7) >> 3; if ((c >> 3) >= per) return false; v = (c & 7) * per + (c >> 3); } }
;         const int L = i * G + v; if (L >= nunits) return false;
;         const int pm = L / NT, pl = L % NT; u.pm = pm; u.pn = tileE[pm] * NT + pl; return true;
;     }
.LBB0_716:
	s_mov_b32 s100, 0
	s_add_i32 s46, s46, 1
	s_mul_i32 s6, s46, s76
	s_and_b64 vcc, exec, s[0:1]
	s_mov_b32 s7, s2
	s_mov_b64 s[4:5], s[12:13]
	s_cbranch_vccnz .LBB0_720
	s_sub_i32 s8, s45, s6
	s_mov_b64 s[4:5], -1
	s_cmp_lt_i32 s8, s76
	s_mov_b32 s7, s85
	s_cbranch_scc0 .LBB0_720
	s_add_i32 s8, s8, 7
	s_ashr_i32 s8, s8, 3
	s_cmp_lt_i32 s44, s8
	s_mov_b64 s[4:5], 0
	s_cbranch_scc0 .LBB0_720
	s_mul_i32 s4, s8, s3
	s_add_i32 s7, s4, s44
	s_mov_b64 s[4:5], -1

; #define PG8_STAGE(bufoff, gbase, voff) do { _Pragma("unroll") for (int _i = 0; _i < 2; ++_i) { unsigned keep_; \
;         asm volatile("s_mov_b32 %0, m0\n\ts_mov_b32 m0, %3\n\ts_nop 0\n\tglobal_load_lds_dwordx4 %1, %2\n\ts_mov_b32 m0, %0" : "=&s"(keep_) : "v"((voff)[_i]), "s"((const char*)(gbase)), "s"(ldsb + (unsigned)((bufoff) + _i * 8192)) : "memory"); } } while (0)
; #define PG8_LDA(dst, b, h) do { _Pragma("unroll") for (int m = 0; m < 4; ++m) _Pragma("unroll") for (int k = 0; k < 2; ++k) dst[m][k] = *(const PG8_LAS bf16x8*)(lds + PG8_SA(b, h) + aoff + m * 2048 + k * 1024); } while (0)
; #define PG8_LDB(dst, b, h) do { _Pragma("unroll") for (int n = 0; n < 2; ++n) _Pragma("unroll") for (int k = 0; k < 2; ++k) dst[n][k] = *(const PG8_LAS bf16x8*)(lds + PG8_SB(b, h) + boff + n * 2048 + k * 1024); } while (0)
; #define PG8_WAIT_V(n) asm volatile("s_waitcnt vmcnt(" #n ")" ::: "memory")
; #define PG8_WAIT_L(n) asm volatile("s_waitcnt lgkmcnt(" #n ")" ::: "memory")
; #define PG8_BAR __builtin_amdgcn_s_barrier()
; #define PG8_SCHED __builtin_amdgcn_sched_barrier(0)
; template <class Epi, class Sched, bool ALIGN_EPI, bool FP8 = false>
; __device__ __forceinline__ void gemm_phase(PG8_LAS unsigned char* lds, const Gemm g, const Sched& S, const Epi& E, const int wid, const int lane) {
;     ...
;             const bool last = (t == nt - 2);
;             const char* a1 = cA + (size_t)(t + 1) * kstep;
;             const char* a2 = last ? nA : cA + (size_t)(t + 2) * kstep; const char* b2 = last ? nB : cB + (size_t)(t + 2) * kstep;
;             const char* a3 = a2 + kstep; const char* b3 = b2 + kstep;
;             PG8_LDB(B0, 0, 0); PG8_LDB(B1, 0, 1); PG8_SCHED; PG8_LDA(At, 0, 0); PG8_STAGE(PG8_SA(1, 1), a1 + hstepA, vc1);
;             if (GA && last && has_next) { const u32x4 q = *gslot; vc0[0] = q.x; vc0[1] = q.y; vc1[0] = q.z; vc1[1] = q.w; }
;             PG8_WAIT_V(8); PG8_WAIT_L(0); PG8_BAR; PG8_MMA(0, 0, At, B0); PG8_MMA(0, 1, At, B1); PG8_BAR; PG8_SCHED;
;             PG8_LDA(At, 0, 1); PG8_STAGE(PG8_SB(0, 0), b2, voffB); PG8_STAGE(PG8_SB(0, 1), b2 + hstep, voffB); PG8_STAGE(PG8_SA(0, 0), a2, vc0);
;             PG8_WAIT_V(8); PG8_WAIT_L(0); PG8_BAR; PG8_MMA(1, 0, At, B0); PG8_MMA(1, 1, At, B1); PG8_BAR; PG8_SCHED;
.LBB0_727:
	s_add_i32 s82, s82, 2
	s_and_b64 s[8:9], s[38:39], exec
	s_cselect_b32 s9, 0, s6
	s_cselect_b32 s8, 0, s7
	s_add_u32 s40, s20, s9
	s_addc_u32 s41, s21, s8
	s_add_u32 s33, s34, s6
	s_addc_u32 s42, s35, s7
	s_add_u32 s8, s40, 0x80
	s_addc_u32 s9, s41, 0
	s_waitcnt vmcnt(8)
	s_and_b64 s[38:39], s[38:39], exec
	s_waitcnt lgkmcnt(0)
	s_cselect_b32 s43, s31, s42
	s_cselect_b32 s42, s30, s33
	s_add_u32 s38, s42, 0x80
	s_addc_u32 s39, s43, 0
	s_barrier
	s_setprio 1
	s_waitcnt lgkmcnt(6)
	v_mfma_scale_f32_16x16x128_f8f6f4 v[192:195], v[24:31], v[56:63], v[192:195], v210, v211 op_sel_hi:[0,0,0]
	v_mfma_scale_f32_16x16x128_f8f6f4 v[184:187], v[16:23], v[56:63], v[184:187], v210, v211 op_sel_hi:[0,0,0]
	s_waitcnt lgkmcnt(4)
	v_mfma_scale_f32_16x16x128_f8f6f4 v[176:179], v[24:31], v[48:55], v[176:179], v210, v211 op_sel_hi:[0,0,0]
	v_mfma_scale_f32_16x16x128_f8f6f4 v[168:171], v[16:23], v[48:55], v[168:171], v210, v211 op_sel_hi:[0,0,0]
	s_waitcnt lgkmcnt(2)
	v_mfma_scale_f32_16x16x128_f8f6f4 v[160:163], v[24:31], v[40:47], v[160:163], v210, v211 op_sel_hi:[0,0,0]
	v_mfma_scale_f32_16x16x128_f8f6f4 v[152:155], v[16:23], v[40:47], v[152:155], v210, v211 op_sel_hi:[0,0,0]
	s_waitcnt lgkmcnt(0)
	v_mfma_scale_f32_16x16x128_f8f6f4 v[144:147], v[24:31], v[32:39], v[144:147], v210, v211 op_sel_hi:[0,0,0]
	v_mfma_scale_f32_16x16x128_f8f6f4 v[136:139], v[16:23], v[32:39], v[136:139], v210, v211 op_sel_hi:[0,0,0]
	s_setprio 0
	s_setprio 1
	v_mfma_scale_f32_16x16x128_f8f6f4 v[188:191], v[8:15], v[56:63], v[188:191], v210, v211 op_sel_hi:[0,0,0]
	v_mfma_scale_f32_16x16x128_f8f6f4 v[180:183], v[0:7], v[56:63], v[180:183], v210, v211 op_sel_hi:[0,0,0]
	v_mfma_scale_f32_16x16x128_f8f6f4 v[172:175], v[8:15], v[48:55], v[172:175], v210, v211 op_sel_hi:[0,0,0]
	v_mfma_scale_f32_16x16x128_f8f6f4 v[164:167], v[0:7], v[48:55], v[164:167], v210, v211 op_sel_hi:[0,0,0]
	v_mfma_scale_f32_16x16x128_f8f6f4 v[156:159], v[8:15], v[40:47], v[156:159], v210, v211 op_sel_hi:[0,0,0]
	v_mfma_scale_f32_16x16x128_f8f6f4 v[148:151], v[0:7], v[40:47], v[148:151], v210, v211 op_sel_hi:[0,0,0]
	v_mfma_scale_f32_16x16x128_f8f6f4 v[140:143], v[8:15], v[32:39], v[140:143], v210, v211 op_sel_hi:[0,0,0]
	v_mfma_scale_f32_16x16x128_f8f6f4 v[132:135], v[0:7], v[32:39], v[132:135], v210, v211 op_sel_hi:[0,0,0]
	s_setprio 0
	s_barrier
	ds_read_b128 v[32:35], v209 offset:16384
	ds_read_b128 v[36:39], v209 offset:17408
	ds_read_b128 v[40:43], v209 offset:18432
	ds_read_b128 v[44:47], v209 offset:19456
	ds_read_b128 v[48:51], v209 offset:20480
	ds_read_b128 v[52:55], v209 offset:21504
	ds_read_b128 v[56:59], v209 offset:22528
	ds_read_b128 v[60:63], v209 offset:23552
	s_mov_b32 m0, s51
	s_nop 0
	global_load_lds_dwordx4 v200, s[42:43]
	s_mov_b32 m0, s53
	s_nop 0
	global_load_lds_dwordx4 v202, s[42:43]
	s_add_u32 s42, s42, s16
	s_addc_u32 s43, s43, s17
	s_mov_b32 m0, s55
	s_nop 0
	global_load_lds_dwordx4 v200, s[42:43]
	s_mov_b32 m0, s64
	s_nop 0
	global_load_lds_dwordx4 v202, s[42:43]
	s_mov_b32 m0, s47
	s_nop 0
	global_load_lds_dwordx4 v64, s[40:41]
	s_mov_b32 m0, s65
	s_nop 0
	global_load_lds_dwordx4 v65, s[40:41]
	s_cmp_eq_u32 s100, 4
	s_cbranch_scc0 .Lp6a_wn
	s_waitcnt vmcnt(12)
	s_mov_b32 s100, 0
	s_branch .Lp6a_wj

; #define PG8_STAGE(bufoff, gbase, voff) do { _Pragma("unroll") for (int _i = 0; _i < 2; ++_i) { unsigned keep_; \
;         asm volatile("s_mov_b32 %0, m0\n\ts_mov_b32 m0, %3\n\ts_nop 0\n\tglobal_load_lds_dwordx4 %1, %2\n\ts_mov_b32 m0, %0" : "=&s"(keep_) : "v"((voff)[_i]), "s"((const char*)(gbase)), "s"(ldsb + (unsigned)((bufoff) + _i * 8192)) : "memory"); } } while (0)
; #define PG8_LDA(dst, b, h) do { _Pragma("unroll") for (int m = 0; m < 4; ++m) _Pragma("unroll") for (int k = 0; k < 2; ++k) dst[m][k] = *(const PG8_LAS bf16x8*)(lds + PG8_SA(b, h) + aoff + m * 2048 + k * 1024); } while (0)
; #define PG8_LDB(dst, b, h) do { _Pragma("unroll") for (int n = 0; n < 2; ++n) _Pragma("unroll") for (int k = 0; k < 2; ++k) dst[n][k] = *(const PG8_LAS bf16x8*)(lds + PG8_SB(b, h) + boff + n * 2048 + k * 1024); } while (0)
; #define PG8_WAIT_V(n) asm volatile("s_waitcnt vmcnt(" #n ")" ::: "memory")
; #define PG8_WAIT_L(n) asm volatile("s_waitcnt lgkmcnt(" #n ")" ::: "memory")
; #define PG8_BAR __builtin_amdgcn_s_barrier()
; #define PG8_SCHED __builtin_amdgcn_sched_barrier(0)
; template <class Epi, class Sched, bool ALIGN_EPI, bool FP8 = false>
; __device__ __forceinline__ void gemm_phase(PG8_LAS unsigned char* lds, const Gemm g, const Sched& S, const Epi& E, const int wid, const int lane) {
;     ...
;             PG8_WAIT_V(8); PG8_WAIT_L(0); PG8_BAR; PG8_MMA(1, 0, At, B0); PG8_MMA(1, 1, At, B1); PG8_BAR; PG8_SCHED;
;             PG8_LDB(B0, 1, 0); PG8_LDB(B1, 1, 1); PG8_SCHED; PG8_LDA(At, 1, 0); PG8_STAGE(PG8_SA(0, 1), a2 + hstepA, vc1);
;             PG8_WAIT_V(8); PG8_WAIT_L(0); PG8_BAR; PG8_MMA(0, 0, At, B0); PG8_MMA(0, 1, At, B1); PG8_BAR; PG8_SCHED;
.Lp6a_wj:
	s_waitcnt lgkmcnt(0)
	s_barrier
	s_setprio 1
	s_waitcnt lgkmcnt(6)
	v_mfma_scale_f32_16x16x128_f8f6f4 v[128:131], v[24:31], v[32:39], v[128:131], v210, v211 op_sel_hi:[0,0,0]
	v_mfma_scale_f32_16x16x128_f8f6f4 v[120:123], v[16:23], v[32:39], v[120:123], v210, v211 op_sel_hi:[0,0,0]
	s_waitcnt lgkmcnt(4)
	v_mfma_scale_f32_16x16x128_f8f6f4 v[112:115], v[24:31], v[40:47], v[112:115], v210, v211 op_sel_hi:[0,0,0]
	v_mfma_scale_f32_16x16x128_f8f6f4 v[104:107], v[16:23], v[40:47], v[104:107], v210, v211 op_sel_hi:[0,0,0]
	s_waitcnt lgkmcnt(2)
	v_mfma_scale_f32_16x16x128_f8f6f4 v[96:99], v[24:31], v[48:55], v[96:99], v210, v211 op_sel_hi:[0,0,0]
	v_mfma_scale_f32_16x16x128_f8f6f4 v[88:91], v[16:23], v[48:55], v[88:91], v210, v211 op_sel_hi:[0,0,0]
	s_waitcnt lgkmcnt(0)
	v_mfma_scale_f32_16x16x128_f8f6f4 v[80:83], v[24:31], v[56:63], v[80:83], v210, v211 op_sel_hi:[0,0,0]
	v_mfma_scale_f32_16x16x128_f8f6f4 v[72:75], v[16:23], v[56:63], v[72:75], v210, v211 op_sel_hi:[0,0,0]
	s_setprio 0
	s_setprio 1
	v_mfma_scale_f32_16x16x128_f8f6f4 v[124:127], v[8:15], v[32:39], v[124:127], v210, v211 op_sel_hi:[0,0,0]
	v_mfma_scale_f32_16x16x128_f8f6f4 v[116:119], v[0:7], v[32:39], v[116:119], v210, v211 op_sel_hi:[0,0,0]
	v_mfma_scale_f32_16x16x128_f8f6f4 v[108:111], v[8:15], v[40:47], v[108:111], v210, v211 op_sel_hi:[0,0,0]
	v_mfma_scale_f32_16x16x128_f8f6f4 v[100:103], v[0:7], v[40:47], v[100:103], v210, v211 op_sel_hi:[0,0,0]
	v_mfma_scale_f32_16x16x128_f8f6f4 v[92:95], v[8:15], v[48:55], v[92:95], v210, v211 op_sel_hi:[0,0,0]
	v_mfma_scale_f32_16x16x128_f8f6f4 v[84:87], v[0:7], v[48:55], v[84:87], v210, v211 op_sel_hi:[0,0,0]
	v_mfma_scale_f32_16x16x128_f8f6f4 v[76:79], v[8:15], v[56:63], v[76:79], v210, v211 op_sel_hi:[0,0,0]
	v_mfma_scale_f32_16x16x128_f8f6f4 v[68:71], v[0:7], v[56:63], v[68:71], v210, v211 op_sel_hi:[0,0,0]
	s_setprio 0
	s_barrier
	v_add_u32_e32 v12, 0x18000, v206
	v_add_u32_e32 v28, 0x1c000, v206
	ds_read_b128 v[0:3], v12
	ds_read_b128 v[4:7], v12 offset:1024
	ds_read_b128 v[8:11], v12 offset:2048
	ds_read_b128 v[12:15], v12 offset:3072
	ds_read_b128 v[16:19], v28
	ds_read_b128 v[20:23], v28 offset:1024
	ds_read_b128 v[24:27], v28 offset:2048
	ds_read_b128 v[28:31], v28 offset:3072
	ds_read_b128 v[32:35], v209 offset:32768
	ds_read_b128 v[36:39], v209 offset:33792
	ds_read_b128 v[40:43], v209 offset:34816
	ds_read_b128 v[44:47], v209 offset:35840
	ds_read_b128 v[48:51], v209 offset:36864
	ds_read_b128 v[52:55], v209 offset:37888
	ds_read_b128 v[56:59], v209 offset:38912
	ds_read_b128 v[60:63], v209 offset:39936
	s_mov_b32 m0, s66
	s_nop 0
	global_load_lds_dwordx4 v66, s[40:41]
	s_mov_b32 m0, s67
	s_nop 0
	global_load_lds_dwordx4 v67, s[40:41]
	s_waitcnt vmcnt(8)
	s_waitcnt lgkmcnt(0)
	s_barrier
	s_setprio 1
	s_waitcnt lgkmcnt(6)
	v_mfma_scale_f32_16x16x128_f8f6f4 v[192:195], v[0:7], v[32:39], v[192:195], v210, v211 op_sel_hi:[0,0,0]
	v_mfma_scale_f32_16x16x128_f8f6f4 v[184:187], v[8:15], v[32:39], v[184:187], v210, v211 op_sel_hi:[0,0,0]
	s_waitcnt lgkmcnt(4)
	v_mfma_scale_f32_16x16x128_f8f6f4 v[176:179], v[0:7], v[40:47], v[176:179], v210, v211 op_sel_hi:[0,0,0]
	v_mfma_scale_f32_16x16x128_f8f6f4 v[168:171], v[8:15], v[40:47], v[168:171], v210, v211 op_sel_hi:[0,0,0]
	s_waitcnt lgkmcnt(2)
	v_mfma_scale_f32_16x16x128_f8f6f4 v[160:163], v[0:7], v[48:55], v[160:163], v210, v211 op_sel_hi:[0,0,0]
	v_mfma_scale_f32_16x16x128_f8f6f4 v[152:155], v[8:15], v[48:55], v[152:155], v210, v211 op_sel_hi:[0,0,0]
	s_waitcnt lgkmcnt(0)
	v_mfma_scale_f32_16x16x128_f8f6f4 v[144:147], v[0:7], v[56:63], v[144:147], v210, v211 op_sel_hi:[0,0,0]
	v_mfma_scale_f32_16x16x128_f8f6f4 v[136:139], v[8:15], v[56:63], v[136:139], v210, v211 op_sel_hi:[0,0,0]
	s_setprio 0
	s_setprio 1
	v_mfma_scale_f32_16x16x128_f8f6f4 v[188:191], v[16:23], v[32:39], v[188:191], v210, v211 op_sel_hi:[0,0,0]
	v_mfma_scale_f32_16x16x128_f8f6f4 v[180:183], v[24:31], v[32:39], v[180:183], v210, v211 op_sel_hi:[0,0,0]
	v_mfma_scale_f32_16x16x128_f8f6f4 v[172:175], v[16:23], v[40:47], v[172:175], v210, v211 op_sel_hi:[0,0,0]
	v_mfma_scale_f32_16x16x128_f8f6f4 v[164:167], v[24:31], v[40:47], v[164:167], v210, v211 op_sel_hi:[0,0,0]
	v_mfma_scale_f32_16x16x128_f8f6f4 v[156:159], v[16:23], v[48:55], v[156:159], v210, v211 op_sel_hi:[0,0,0]
	v_mfma_scale_f32_16x16x128_f8f6f4 v[148:151], v[24:31], v[48:55], v[148:151], v210, v211 op_sel_hi:[0,0,0]
	v_mfma_scale_f32_16x16x128_f8f6f4 v[140:143], v[16:23], v[56:63], v[140:143], v210, v211 op_sel_hi:[0,0,0]
	v_mfma_scale_f32_16x16x128_f8f6f4 v[132:135], v[24:31], v[56:63], v[132:135], v210, v211 op_sel_hi:[0,0,0]
	s_setprio 0
	s_barrier
; #define PG8_STAGE(bufoff, gbase, voff) do { _Pragma("unroll") for (int _i = 0; _i < 2; ++_i) { unsigned keep_; \
;         asm volatile("s_mov_b32 %0, m0\n\ts_mov_b32 m0, %3\n\ts_nop 0\n\tglobal_load_lds_dwordx4 %1, %2\n\ts_mov_b32 m0, %0" : "=&s"(keep_) : "v"((voff)[_i]), "s"((const char*)(gbase)), "s"(ldsb + (unsigned)((bufoff) + _i * 8192)) : "memory"); } } while (0)
; #define PG8_LDA(dst, b, h) do { _Pragma("unroll") for (int m = 0; m < 4; ++m) _Pragma("unroll") for (int k = 0; k < 2; ++k) dst[m][k] = *(const PG8_LAS bf16x8*)(lds + PG8_SA(b, h) + aoff + m * 2048 + k * 1024); } while (0)
; #define PG8_LDB(dst, b, h) do { _Pragma("unroll") for (int n = 0; n < 2; ++n) _Pragma("unroll") for (int k = 0; k < 2; ++k) dst[n][k] = *(const PG8_LAS bf16x8*)(lds + PG8_SB(b, h) + boff + n * 2048 + k * 1024); } while (0)
; #define PG8_WAIT_V(n) asm volatile("s_waitcnt vmcnt(" #n ")" ::: "memory")
; #define PG8_WAIT_L(n) asm volatile("s_waitcnt lgkmcnt(" #n ")" ::: "memory")
; #define PG8_BAR __builtin_amdgcn_s_barrier()
; #define PG8_SCHED __builtin_amdgcn_sched_barrier(0)
; template <class Epi, class Sched, bool ALIGN_EPI, bool FP8 = false>
; __device__ __forceinline__ void gemm_phase(PG8_LAS unsigned char* lds, const Gemm g, const Sched& S, const Epi& E, const int wid, const int lane) {
;     ...
;         for (int t = 0; t < nt; t += 2) {
;             const bool last = (t == nt - 2);
;             const char* a1 = cA + (size_t)(t + 1) * kstep;
;             const char* a2 = last ? nA : cA + (size_t)(t + 2) * kstep; const char* b2 = last ? nB : cB + (size_t)(t + 2) * kstep;
;             const char* a3 = a2 + kstep; const char* b3 = b2 + kstep;
;             PG8_LDB(B0, 0, 0); PG8_LDB(B1, 0, 1); PG8_SCHED; PG8_LDA(At, 0, 0); PG8_STAGE(PG8_SA(1, 1), a1 + hstepA, vc1);
;             if (GA && last && has_next) { const u32x4 q = *gslot; vc0[0] = q.x; vc0[1] = q.y; vc1[0] = q.z; vc1[1] = q.w; }
;     ...
;             PG8_LDA(At, 1, 1); PG8_STAGE(PG8_SB(1, 0), b3, voffB); PG8_STAGE(PG8_SB(1, 1), b3 + hstep, voffB); PG8_STAGE(PG8_SA(1, 0), a3, vc0);
;             PG8_WAIT_V(8); PG8_WAIT_L(0); PG8_BAR; PG8_MMA(1, 0, At, B0); PG8_MMA(1, 1, At, B1); PG8_BAR; PG8_SCHED;
	ds_read_b128 v[32:35], v209 offset:49152
	ds_read_b128 v[36:39], v209 offset:50176
	ds_read_b128 v[40:43], v209 offset:51200
	ds_read_b128 v[44:47], v209 offset:52224
	ds_read_b128 v[48:51], v209 offset:53248
	ds_read_b128 v[52:55], v209 offset:54272
	ds_read_b128 v[56:59], v209 offset:55296
	ds_read_b128 v[60:63], v209 offset:56320
	s_mov_b32 m0, s69
	s_nop 0
	global_load_lds_dwordx4 v200, s[38:39]
	s_mov_b32 m0, s70
	s_nop 0
	global_load_lds_dwordx4 v202, s[38:39]
	s_add_u32 s38, s38, s16
	s_addc_u32 s39, s39, s17
	s_mov_b32 m0, s73
	s_nop 0
	global_load_lds_dwordx4 v200, s[38:39]
	s_mov_b32 m0, s74
	s_nop 0
	global_load_lds_dwordx4 v202, s[38:39]
	s_mov_b32 m0, s71
	s_nop 0
	global_load_lds_dwordx4 v64, s[8:9]
	s_mov_b32 m0, s72
	s_nop 0
	global_load_lds_dwordx4 v65, s[8:9]
	s_waitcnt vmcnt(8)
	s_waitcnt lgkmcnt(0)
	s_barrier
	s_setprio 1
	s_waitcnt lgkmcnt(6)
	v_mfma_scale_f32_16x16x128_f8f6f4 v[128:131], v[0:7], v[32:39], v[128:131], v210, v211 op_sel_hi:[0,0,0]
	v_mfma_scale_f32_16x16x128_f8f6f4 v[120:123], v[8:15], v[32:39], v[120:123], v210, v211 op_sel_hi:[0,0,0]
	s_waitcnt lgkmcnt(4)
	v_mfma_scale_f32_16x16x128_f8f6f4 v[112:115], v[0:7], v[40:47], v[112:115], v210, v211 op_sel_hi:[0,0,0]
	v_mfma_scale_f32_16x16x128_f8f6f4 v[104:107], v[8:15], v[40:47], v[104:107], v210, v211 op_sel_hi:[0,0,0]
	s_waitcnt lgkmcnt(2)
	v_mfma_scale_f32_16x16x128_f8f6f4 v[96:99], v[0:7], v[48:55], v[96:99], v210, v211 op_sel_hi:[0,0,0]
	v_mfma_scale_f32_16x16x128_f8f6f4 v[88:91], v[8:15], v[48:55], v[88:91], v210, v211 op_sel_hi:[0,0,0]
	s_waitcnt lgkmcnt(0)
	v_mfma_scale_f32_16x16x128_f8f6f4 v[80:83], v[0:7], v[56:63], v[80:83], v210, v211 op_sel_hi:[0,0,0]
	v_mfma_scale_f32_16x16x128_f8f6f4 v[72:75], v[8:15], v[56:63], v[72:75], v210, v211 op_sel_hi:[0,0,0]
	s_setprio 0
	s_setprio 1
	v_mfma_scale_f32_16x16x128_f8f6f4 v[124:127], v[16:23], v[32:39], v[124:127], v210, v211 op_sel_hi:[0,0,0]
	v_mfma_scale_f32_16x16x128_f8f6f4 v[116:119], v[24:31], v[32:39], v[116:119], v210, v211 op_sel_hi:[0,0,0]
	v_mfma_scale_f32_16x16x128_f8f6f4 v[108:111], v[16:23], v[40:47], v[108:111], v210, v211 op_sel_hi:[0,0,0]
	v_mfma_scale_f32_16x16x128_f8f6f4 v[100:103], v[24:31], v[40:47], v[100:103], v210, v211 op_sel_hi:[0,0,0]
	v_mfma_scale_f32_16x16x128_f8f6f4 v[92:95], v[16:23], v[48:55], v[92:95], v210, v211 op_sel_hi:[0,0,0]
	v_mfma_scale_f32_16x16x128_f8f6f4 v[84:87], v[24:31], v[48:55], v[84:87], v210, v211 op_sel_hi:[0,0,0]
	v_mfma_scale_f32_16x16x128_f8f6f4 v[76:79], v[16:23], v[56:63], v[76:79], v210, v211 op_sel_hi:[0,0,0]
	v_mfma_scale_f32_16x16x128_f8f6f4 v[68:71], v[24:31], v[56:63], v[68:71], v210, v211 op_sel_hi:[0,0,0]
	s_setprio 0
	s_barrier
	s_add_u32 s6, s6, 0x100
	s_addc_u32 s7, s7, 0
	s_cmp_ge_i32 s82, s68
	s_cbranch_scc1 .LBB0_749
.LBB0_728:
	ds_read_b128 v[24:27], v207
	ds_read_b128 v[28:31], v207 offset:1024
	ds_read_b128 v[16:19], v207 offset:2048
	ds_read_b128 v[20:23], v207 offset:3072
	ds_read_b128 v[8:11], v208
	ds_read_b128 v[12:15], v208 offset:1024
	ds_read_b128 v[0:3], v208 offset:2048
	ds_read_b128 v[4:7], v208 offset:3072
	s_cmp_eq_u32 s75, s82
	s_cselect_b64 s[38:39], -1, 0
	s_add_u32 s8, s20, s6
	s_addc_u32 s9, s21, s7
	s_add_u32 s8, s8, 0xffffff80
	s_addc_u32 s9, s9, -1
	ds_read_b128 v[56:59], v209
	ds_read_b128 v[60:63], v209 offset:1024
	ds_read_b128 v[48:51], v209 offset:2048
	ds_read_b128 v[52:55], v209 offset:3072
	ds_read_b128 v[40:43], v209 offset:4096
	ds_read_b128 v[44:47], v209 offset:5120
	ds_read_b128 v[32:35], v209 offset:6144
	ds_read_b128 v[36:39], v209 offset:7168
	s_mov_b32 m0, s83
	s_nop 0
	global_load_lds_dwordx4 v66, s[8:9]
	s_and_b64 s[40:41], s[36:37], s[38:39]
	s_mov_b32 m0, s84
	s_nop 0
	global_load_lds_dwordx4 v67, s[8:9]
	s_andn2_b64 vcc, exec, s[40:41]
	s_cbranch_vccnz .LBB0_727
	v_lshl_add_u32 v64, v224, 11, v198
	v_lshl_add_u32 v65, v225, 11, v196
	v_lshl_add_u32 v66, v226, 11, v198
	v_lshl_add_u32 v67, v227, 11, v196
	s_branch .LBB0_727

; template <class Epi, class Sched, bool ALIGN_EPI, bool FP8 = false>
; __device__ __forceinline__ void gemm_phase(PG8_LAS unsigned char* lds, const Gemm g, const Sched& S, const Epi& E, const int wid, const int lane) {
;     ...
;         if (GA && has_next) {
;             u32x4 q; q.x = S.tok_off(nxt, rA[0]) + cA2[0]; q.y = S.tok_off(nxt, rA[1]) + cA2[1]; q.z = S.tok_off(nxt, HALF + rA[0]) + cA2[0]; q.w = S.tok_off(nxt, HALF + rA[1]) + cA2[1];
;             *gslot = q;
;     __device__ __forceinline__ unsigned tok_off(const Unit& u, int r) const {
;         const int e = tileE[u.pm], local = (u.pm - tb[e]) * 256 + r;
;         int tok = local;
;         if (e < NE) tok = (local < cnt[e]) ? list[(size_t)e * LISTCAP + local] : 0;
;         return (unsigned)tok * K2;
;     }
.LBB0_731:
	s_lshl_b32 s6, s86, 2
	s_add_i32 s6, s6, 0x20800
	v_mov_b32_e32 v0, s6
	ds_read_b32 v1, v0
	s_waitcnt lgkmcnt(0)
	s_nop 0
	v_readfirstlane_b32 s38, v1
	s_nop 3
	s_lshl_b32 s6, s38, 2
	s_add_i32 s7, s6, 0x21000
	s_add_i32 s6, s6, 0x21200
	v_mov_b32_e32 v0, s7
	v_mov_b32_e32 v1, s6
	ds_read_b32 v0, v0
	ds_read_b32 v1, v1
	s_waitcnt lgkmcnt(0)
	v_sub_u32_e32 v0, s86, v0
	v_lshlrev_b32_e32 v4, 8, v0
	v_or_b32_e32 v6, 0x80, v4
	v_add_u32_e32 v0, v4, v199
	v_add_u32_e32 v2, v4, v204
	v_add_u32_e32 v4, v6, v199
	v_add_u32_e32 v6, v6, v204
	v_mov_b32_e32 v224, v0
	v_mov_b32_e32 v225, v2
	v_mov_b32_e32 v226, v4
	v_mov_b32_e32 v227, v6
	s_cmp_gt_i32 s38, 63
	s_cbranch_scc1 .LBB0_747
	s_ashr_i32 s39, s38, 31
	s_lshl_b64 s[40:41], s[38:39], 16
	s_add_u32 s40, s14, s40
	s_addc_u32 s41, s15, s41
	v_cmp_lt_i32_e32 vcc, v0, v1
	v_lshlrev_b32_e32 v220, 2, v0
	v_mov_b32_e32 v224, 0
	s_and_saveexec_b64 s[6:7], vcc
	s_cbranch_execz .Lp6a_g0
	global_load_dword v224, v220, s[40:41]
	s_add_i32 s100, s100, 1
.Lp6a_g0:
	s_or_b64 exec, exec, s[6:7]
	v_cmp_lt_i32_e32 vcc, v2, v1
	v_lshlrev_b32_e32 v221, 2, v2
	v_mov_b32_e32 v225, 0
	s_and_saveexec_b64 s[6:7], vcc
	s_cbranch_execz .Lp6a_g1
	global_load_dword v225, v221, s[40:41]
	s_add_i32 s100, s100, 1
.Lp6a_g1:
	s_or_b64 exec, exec, s[6:7]
	v_cmp_lt_i32_e32 vcc, v4, v1
	v_lshlrev_b32_e32 v222, 2, v4
	v_mov_b32_e32 v226, 0
	s_and_saveexec_b64 s[6:7], vcc
	s_cbranch_execz .Lp6a_g2
	global_load_dword v226, v222, s[40:41]
	s_add_i32 s100, s100, 1
.Lp6a_g2:
	s_or_b64 exec, exec, s[6:7]
	v_cmp_lt_i32_e32 vcc, v6, v1
	v_lshlrev_b32_e32 v223, 2, v6
	v_mov_b32_e32 v227, 0
	s_and_saveexec_b64 s[6:7], vcc
	s_cbranch_execz .Lp6a_g3
	global_load_dword v227, v223, s[40:41]
	s_add_i32 s100, s100, 1

; template <class Epi, class Sched, bool ALIGN_EPI, bool FP8 = false>
; __device__ __forceinline__ void gemm_phase(PG8_LAS unsigned char* lds, const Gemm g, const Sched& S, const Epi& E, const int wid, const int lane) {
;     ...
;         if (GA && has_next) {
;             u32x4 q; q.x = S.tok_off(nxt, rA[0]) + cA2[0]; q.y = S.tok_off(nxt, rA[1]) + cA2[1]; q.z = S.tok_off(nxt, HALF + rA[0]) + cA2[0]; q.w = S.tok_off(nxt, HALF + rA[1]) + cA2[1];
;             *gslot = q;
;         }
.LBB0_747:
	s_andn2_b64 vcc, exec, s[26:27]
	v_mov_b32_e32 v195, 0
	s_cbranch_vccz .LBB0_726

;     __device__ __forceinline__ bool next(int i, Unit& u) const {
;         int v = c;
;         if ((G & 7) == 0) { const int rem = nunits - i * G;
;             if (rem >= G) v = (c & 7) * (G >> 3) + (c >> 3);
;             else { const int per = (rem + 7) >> 3; if ((c >> 3) >= per) return false; v = (c & 7) * per + (c >> 3); } }
;         const int L = i * G + v; if (L >= nunits) return false;
;         const int pm = L / NT, pl = L % NT; u.pm = pm; u.pn = tileE[pm] * NT + pl; return true;
;     }
.LBB0_1626:
	s_mov_b32 s100, 0
	s_add_i32 s46, s46, 1
	s_mul_i32 s6, s46, s76
	s_and_b64 vcc, exec, s[0:1]
	s_mov_b32 s7, s2
	s_mov_b64 s[4:5], s[12:13]
	s_cbranch_vccnz .LBB0_1630
	s_sub_i32 s8, s45, s6
	s_mov_b64 s[4:5], -1
	s_cmp_lt_i32 s8, s76
	s_mov_b32 s7, s84
	s_cbranch_scc0 .LBB0_1630
	s_add_i32 s8, s8, 7
	s_ashr_i32 s8, s8, 3
	s_cmp_lt_i32 s44, s8
	s_mov_b64 s[4:5], 0
	s_cbranch_scc0 .LBB0_1630
	s_mul_i32 s4, s8, s3
	s_add_i32 s7, s4, s44
	s_mov_b64 s[4:5], -1

; #define PG8_STAGE(bufoff, gbase, voff) do { _Pragma("unroll") for (int _i = 0; _i < 2; ++_i) { unsigned keep_; \
;         asm volatile("s_mov_b32 %0, m0\n\ts_mov_b32 m0, %3\n\ts_nop 0\n\tglobal_load_lds_dwordx4 %1, %2\n\ts_mov_b32 m0, %0" : "=&s"(keep_) : "v"((voff)[_i]), "s"((const char*)(gbase)), "s"(ldsb + (unsigned)((bufoff) + _i * 8192)) : "memory"); } } while (0)
; #define PG8_LDA(dst, b, h) do { _Pragma("unroll") for (int m = 0; m < 4; ++m) _Pragma("unroll") for (int k = 0; k < 2; ++k) dst[m][k] = *(const PG8_LAS bf16x8*)(lds + PG8_SA(b, h) + aoff + m * 2048 + k * 1024); } while (0)
; #define PG8_LDB(dst, b, h) do { _Pragma("unroll") for (int n = 0; n < 2; ++n) _Pragma("unroll") for (int k = 0; k < 2; ++k) dst[n][k] = *(const PG8_LAS bf16x8*)(lds + PG8_SB(b, h) + boff + n * 2048 + k * 1024); } while (0)
; #define PG8_WAIT_V(n) asm volatile("s_waitcnt vmcnt(" #n ")" ::: "memory")
; #define PG8_WAIT_L(n) asm volatile("s_waitcnt lgkmcnt(" #n ")" ::: "memory")
; #define PG8_BAR __builtin_amdgcn_s_barrier()
; #define PG8_SCHED __builtin_amdgcn_sched_barrier(0)
; template <class Epi, class Sched, bool ALIGN_EPI, bool FP8 = false>
; __device__ __forceinline__ void gemm_phase(PG8_LAS unsigned char* lds, const Gemm g, const Sched& S, const Epi& E, const int wid, const int lane) {
;     ...
;             const bool last = (t == nt - 2);
;             const char* a1 = cA + (size_t)(t + 1) * kstep;
;             const char* a2 = last ? nA : cA + (size_t)(t + 2) * kstep; const char* b2 = last ? nB : cB + (size_t)(t + 2) * kstep;
;             const char* a3 = a2 + kstep; const char* b3 = b2 + kstep;
;             PG8_LDB(B0, 0, 0); PG8_LDB(B1, 0, 1); PG8_SCHED; PG8_LDA(At, 0, 0); PG8_STAGE(PG8_SA(1, 1), a1 + hstepA, vc1);
;             if (GA && last && has_next) { const u32x4 q = *gslot; vc0[0] = q.x; vc0[1] = q.y; vc1[0] = q.z; vc1[1] = q.w; }
;             PG8_WAIT_V(8); PG8_WAIT_L(0); PG8_BAR; PG8_MMA(0, 0, At, B0); PG8_MMA(0, 1, At, B1); PG8_BAR; PG8_SCHED;
;             PG8_LDA(At, 0, 1); PG8_STAGE(PG8_SB(0, 0), b2, voffB); PG8_STAGE(PG8_SB(0, 1), b2 + hstep, voffB); PG8_STAGE(PG8_SA(0, 0), a2, vc0);
;             PG8_WAIT_V(8); PG8_WAIT_L(0); PG8_BAR; PG8_MMA(1, 0, At, B0); PG8_MMA(1, 1, At, B1); PG8_BAR; PG8_SCHED;
.LBB0_1637:
	s_add_i32 s89, s89, 2
	s_and_b64 s[8:9], s[38:39], exec
	s_cselect_b32 s9, 0, s6
	s_cselect_b32 s8, 0, s7
	s_add_u32 s40, s20, s9
	s_addc_u32 s41, s21, s8
	s_add_u32 s33, s34, s6
	s_addc_u32 s42, s35, s7
	s_add_u32 s8, s40, 0x80
	s_addc_u32 s9, s41, 0
	s_waitcnt vmcnt(8)
	s_and_b64 s[38:39], s[38:39], exec
	s_waitcnt lgkmcnt(0)
	s_cselect_b32 s43, s31, s42
	s_cselect_b32 s42, s30, s33
	s_add_u32 s38, s42, 0x80
	s_addc_u32 s39, s43, 0
	s_barrier
	s_setprio 1
	s_waitcnt lgkmcnt(6)
	v_mfma_scale_f32_16x16x128_f8f6f4 v[192:195], v[24:31], v[56:63], v[192:195], v210, v211 op_sel_hi:[0,0,0]
	v_mfma_scale_f32_16x16x128_f8f6f4 v[184:187], v[16:23], v[56:63], v[184:187], v210, v211 op_sel_hi:[0,0,0]
	s_waitcnt lgkmcnt(4)
	v_mfma_scale_f32_16x16x128_f8f6f4 v[176:179], v[24:31], v[48:55], v[176:179], v210, v211 op_sel_hi:[0,0,0]
	v_mfma_scale_f32_16x16x128_f8f6f4 v[168:171], v[16:23], v[48:55], v[168:171], v210, v211 op_sel_hi:[0,0,0]
	s_waitcnt lgkmcnt(2)
	v_mfma_scale_f32_16x16x128_f8f6f4 v[160:163], v[24:31], v[40:47], v[160:163], v210, v211 op_sel_hi:[0,0,0]
	v_mfma_scale_f32_16x16x128_f8f6f4 v[152:155], v[16:23], v[40:47], v[152:155], v210, v211 op_sel_hi:[0,0,0]
	s_waitcnt lgkmcnt(0)
	v_mfma_scale_f32_16x16x128_f8f6f4 v[144:147], v[24:31], v[32:39], v[144:147], v210, v211 op_sel_hi:[0,0,0]
	v_mfma_scale_f32_16x16x128_f8f6f4 v[136:139], v[16:23], v[32:39], v[136:139], v210, v211 op_sel_hi:[0,0,0]
	s_setprio 0
	s_setprio 1
	v_mfma_scale_f32_16x16x128_f8f6f4 v[188:191], v[8:15], v[56:63], v[188:191], v210, v211 op_sel_hi:[0,0,0]
	v_mfma_scale_f32_16x16x128_f8f6f4 v[180:183], v[0:7], v[56:63], v[180:183], v210, v211 op_sel_hi:[0,0,0]
	v_mfma_scale_f32_16x16x128_f8f6f4 v[172:175], v[8:15], v[48:55], v[172:175], v210, v211 op_sel_hi:[0,0,0]
	v_mfma_scale_f32_16x16x128_f8f6f4 v[164:167], v[0:7], v[48:55], v[164:167], v210, v211 op_sel_hi:[0,0,0]
	v_mfma_scale_f32_16x16x128_f8f6f4 v[156:159], v[8:15], v[40:47], v[156:159], v210, v211 op_sel_hi:[0,0,0]
	v_mfma_scale_f32_16x16x128_f8f6f4 v[148:151], v[0:7], v[40:47], v[148:151], v210, v211 op_sel_hi:[0,0,0]
	v_mfma_scale_f32_16x16x128_f8f6f4 v[140:143], v[8:15], v[32:39], v[140:143], v210, v211 op_sel_hi:[0,0,0]
	v_mfma_scale_f32_16x16x128_f8f6f4 v[132:135], v[0:7], v[32:39], v[132:135], v210, v211 op_sel_hi:[0,0,0]
	s_setprio 0
	s_barrier
	ds_read_b128 v[32:35], v209 offset:16384
	ds_read_b128 v[36:39], v209 offset:17408
	ds_read_b128 v[40:43], v209 offset:18432
	ds_read_b128 v[44:47], v209 offset:19456
	ds_read_b128 v[48:51], v209 offset:20480
	ds_read_b128 v[52:55], v209 offset:21504
	ds_read_b128 v[56:59], v209 offset:22528
	ds_read_b128 v[60:63], v209 offset:23552
	s_mov_b32 m0, s51
	s_nop 0
	global_load_lds_dwordx4 v200, s[42:43]
	s_mov_b32 m0, s53
	s_nop 0
	global_load_lds_dwordx4 v202, s[42:43]
	s_add_u32 s42, s42, s16
	s_addc_u32 s43, s43, s17
	s_mov_b32 m0, s55
	s_nop 0
	global_load_lds_dwordx4 v200, s[42:43]
	s_mov_b32 m0, s64
	s_nop 0
	global_load_lds_dwordx4 v202, s[42:43]
	s_mov_b32 m0, s47
	s_nop 0
	global_load_lds_dwordx4 v64, s[40:41]
	s_mov_b32 m0, s65
	s_nop 0
	global_load_lds_dwordx4 v65, s[40:41]
	s_cmp_eq_u32 s100, 4
	s_cbranch_scc0 .Lp6b_wn
	s_waitcnt vmcnt(12)
	s_mov_b32 s100, 0
	s_branch .Lp6b_wj

; #define PG8_STAGE(bufoff, gbase, voff) do { _Pragma("unroll") for (int _i = 0; _i < 2; ++_i) { unsigned keep_; \
;         asm volatile("s_mov_b32 %0, m0\n\ts_mov_b32 m0, %3\n\ts_nop 0\n\tglobal_load_lds_dwordx4 %1, %2\n\ts_mov_b32 m0, %0" : "=&s"(keep_) : "v"((voff)[_i]), "s"((const char*)(gbase)), "s"(ldsb + (unsigned)((bufoff) + _i * 8192)) : "memory"); } } while (0)
; #define PG8_LDA(dst, b, h) do { _Pragma("unroll") for (int m = 0; m < 4; ++m) _Pragma("unroll") for (int k = 0; k < 2; ++k) dst[m][k] = *(const PG8_LAS bf16x8*)(lds + PG8_SA(b, h) + aoff + m * 2048 + k * 1024); } while (0)
; #define PG8_LDB(dst, b, h) do { _Pragma("unroll") for (int n = 0; n < 2; ++n) _Pragma("unroll") for (int k = 0; k < 2; ++k) dst[n][k] = *(const PG8_LAS bf16x8*)(lds + PG8_SB(b, h) + boff + n * 2048 + k * 1024); } while (0)
; #define PG8_WAIT_V(n) asm volatile("s_waitcnt vmcnt(" #n ")" ::: "memory")
; #define PG8_WAIT_L(n) asm volatile("s_waitcnt lgkmcnt(" #n ")" ::: "memory")
; #define PG8_BAR __builtin_amdgcn_s_barrier()
; #define PG8_SCHED __builtin_amdgcn_sched_barrier(0)
; template <class Epi, class Sched, bool ALIGN_EPI, bool FP8 = false>
; __device__ __forceinline__ void gemm_phase(PG8_LAS unsigned char* lds, const Gemm g, const Sched& S, const Epi& E, const int wid, const int lane) {
;     ...
;             PG8_WAIT_V(8); PG8_WAIT_L(0); PG8_BAR; PG8_MMA(1, 0, At, B0); PG8_MMA(1, 1, At, B1); PG8_BAR; PG8_SCHED;
;             PG8_LDB(B0, 1, 0); PG8_LDB(B1, 1, 1); PG8_SCHED; PG8_LDA(At, 1, 0); PG8_STAGE(PG8_SA(0, 1), a2 + hstepA, vc1);
;             PG8_WAIT_V(8); PG8_WAIT_L(0); PG8_BAR; PG8_MMA(0, 0, At, B0); PG8_MMA(0, 1, At, B1); PG8_BAR; PG8_SCHED;
.Lp6b_wj:
	s_waitcnt lgkmcnt(0)
	s_barrier
	s_setprio 1
	s_waitcnt lgkmcnt(6)
	v_mfma_scale_f32_16x16x128_f8f6f4 v[128:131], v[24:31], v[32:39], v[128:131], v210, v211 op_sel_hi:[0,0,0]
	v_mfma_scale_f32_16x16x128_f8f6f4 v[120:123], v[16:23], v[32:39], v[120:123], v210, v211 op_sel_hi:[0,0,0]
	s_waitcnt lgkmcnt(4)
	v_mfma_scale_f32_16x16x128_f8f6f4 v[112:115], v[24:31], v[40:47], v[112:115], v210, v211 op_sel_hi:[0,0,0]
	v_mfma_scale_f32_16x16x128_f8f6f4 v[104:107], v[16:23], v[40:47], v[104:107], v210, v211 op_sel_hi:[0,0,0]
	s_waitcnt lgkmcnt(2)
	v_mfma_scale_f32_16x16x128_f8f6f4 v[96:99], v[24:31], v[48:55], v[96:99], v210, v211 op_sel_hi:[0,0,0]
	v_mfma_scale_f32_16x16x128_f8f6f4 v[88:91], v[16:23], v[48:55], v[88:91], v210, v211 op_sel_hi:[0,0,0]
	s_waitcnt lgkmcnt(0)
	v_mfma_scale_f32_16x16x128_f8f6f4 v[80:83], v[24:31], v[56:63], v[80:83], v210, v211 op_sel_hi:[0,0,0]
	v_mfma_scale_f32_16x16x128_f8f6f4 v[72:75], v[16:23], v[56:63], v[72:75], v210, v211 op_sel_hi:[0,0,0]
	s_setprio 0
	s_setprio 1
	v_mfma_scale_f32_16x16x128_f8f6f4 v[124:127], v[8:15], v[32:39], v[124:127], v210, v211 op_sel_hi:[0,0,0]
	v_mfma_scale_f32_16x16x128_f8f6f4 v[116:119], v[0:7], v[32:39], v[116:119], v210, v211 op_sel_hi:[0,0,0]
	v_mfma_scale_f32_16x16x128_f8f6f4 v[108:111], v[8:15], v[40:47], v[108:111], v210, v211 op_sel_hi:[0,0,0]
	v_mfma_scale_f32_16x16x128_f8f6f4 v[100:103], v[0:7], v[40:47], v[100:103], v210, v211 op_sel_hi:[0,0,0]
	v_mfma_scale_f32_16x16x128_f8f6f4 v[92:95], v[8:15], v[48:55], v[92:95], v210, v211 op_sel_hi:[0,0,0]
	v_mfma_scale_f32_16x16x128_f8f6f4 v[84:87], v[0:7], v[48:55], v[84:87], v210, v211 op_sel_hi:[0,0,0]
	v_mfma_scale_f32_16x16x128_f8f6f4 v[76:79], v[8:15], v[56:63], v[76:79], v210, v211 op_sel_hi:[0,0,0]
	v_mfma_scale_f32_16x16x128_f8f6f4 v[68:71], v[0:7], v[56:63], v[68:71], v210, v211 op_sel_hi:[0,0,0]
	s_setprio 0
	s_barrier
	v_add_u32_e32 v12, 0x18000, v206
	v_add_u32_e32 v28, 0x1c000, v206
	ds_read_b128 v[0:3], v12
	ds_read_b128 v[4:7], v12 offset:1024
	ds_read_b128 v[8:11], v12 offset:2048
	ds_read_b128 v[12:15], v12 offset:3072
	ds_read_b128 v[16:19], v28
	ds_read_b128 v[20:23], v28 offset:1024
	ds_read_b128 v[24:27], v28 offset:2048
	ds_read_b128 v[28:31], v28 offset:3072
	ds_read_b128 v[32:35], v209 offset:32768
	ds_read_b128 v[36:39], v209 offset:33792
	ds_read_b128 v[40:43], v209 offset:34816
	ds_read_b128 v[44:47], v209 offset:35840
	ds_read_b128 v[48:51], v209 offset:36864
	ds_read_b128 v[52:55], v209 offset:37888
	ds_read_b128 v[56:59], v209 offset:38912
	ds_read_b128 v[60:63], v209 offset:39936
	s_mov_b32 m0, s66
	s_nop 0
	global_load_lds_dwordx4 v66, s[40:41]
	s_mov_b32 m0, s67
	s_nop 0
	global_load_lds_dwordx4 v67, s[40:41]
	s_waitcnt vmcnt(8)
	s_waitcnt lgkmcnt(0)
	s_barrier
	s_setprio 1
	s_waitcnt lgkmcnt(6)
	v_mfma_scale_f32_16x16x128_f8f6f4 v[192:195], v[0:7], v[32:39], v[192:195], v210, v211 op_sel_hi:[0,0,0]
	v_mfma_scale_f32_16x16x128_f8f6f4 v[184:187], v[8:15], v[32:39], v[184:187], v210, v211 op_sel_hi:[0,0,0]
	s_waitcnt lgkmcnt(4)
	v_mfma_scale_f32_16x16x128_f8f6f4 v[176:179], v[0:7], v[40:47], v[176:179], v210, v211 op_sel_hi:[0,0,0]
	v_mfma_scale_f32_16x16x128_f8f6f4 v[168:171], v[8:15], v[40:47], v[168:171], v210, v211 op_sel_hi:[0,0,0]
	s_waitcnt lgkmcnt(2)
	v_mfma_scale_f32_16x16x128_f8f6f4 v[160:163], v[0:7], v[48:55], v[160:163], v210, v211 op_sel_hi:[0,0,0]
	v_mfma_scale_f32_16x16x128_f8f6f4 v[152:155], v[8:15], v[48:55], v[152:155], v210, v211 op_sel_hi:[0,0,0]
	s_waitcnt lgkmcnt(0)
	v_mfma_scale_f32_16x16x128_f8f6f4 v[144:147], v[0:7], v[56:63], v[144:147], v210, v211 op_sel_hi:[0,0,0]
	v_mfma_scale_f32_16x16x128_f8f6f4 v[136:139], v[8:15], v[56:63], v[136:139], v210, v211 op_sel_hi:[0,0,0]
	s_setprio 0
	s_setprio 1
	v_mfma_scale_f32_16x16x128_f8f6f4 v[188:191], v[16:23], v[32:39], v[188:191], v210, v211 op_sel_hi:[0,0,0]
	v_mfma_scale_f32_16x16x128_f8f6f4 v[180:183], v[24:31], v[32:39], v[180:183], v210, v211 op_sel_hi:[0,0,0]
	v_mfma_scale_f32_16x16x128_f8f6f4 v[172:175], v[16:23], v[40:47], v[172:175], v210, v211 op_sel_hi:[0,0,0]
	v_mfma_scale_f32_16x16x128_f8f6f4 v[164:167], v[24:31], v[40:47], v[164:167], v210, v211 op_sel_hi:[0,0,0]
	v_mfma_scale_f32_16x16x128_f8f6f4 v[156:159], v[16:23], v[48:55], v[156:159], v210, v211 op_sel_hi:[0,0,0]
	v_mfma_scale_f32_16x16x128_f8f6f4 v[148:151], v[24:31], v[48:55], v[148:151], v210, v211 op_sel_hi:[0,0,0]
	v_mfma_scale_f32_16x16x128_f8f6f4 v[140:143], v[16:23], v[56:63], v[140:143], v210, v211 op_sel_hi:[0,0,0]
	v_mfma_scale_f32_16x16x128_f8f6f4 v[132:135], v[24:31], v[56:63], v[132:135], v210, v211 op_sel_hi:[0,0,0]
	s_setprio 0
	s_barrier
; #define PG8_STAGE(bufoff, gbase, voff) do { _Pragma("unroll") for (int _i = 0; _i < 2; ++_i) { unsigned keep_; \
;         asm volatile("s_mov_b32 %0, m0\n\ts_mov_b32 m0, %3\n\ts_nop 0\n\tglobal_load_lds_dwordx4 %1, %2\n\ts_mov_b32 m0, %0" : "=&s"(keep_) : "v"((voff)[_i]), "s"((const char*)(gbase)), "s"(ldsb + (unsigned)((bufoff) + _i * 8192)) : "memory"); } } while (0)
; #define PG8_LDA(dst, b, h) do { _Pragma("unroll") for (int m = 0; m < 4; ++m) _Pragma("unroll") for (int k = 0; k < 2; ++k) dst[m][k] = *(const PG8_LAS bf16x8*)(lds + PG8_SA(b, h) + aoff + m * 2048 + k * 1024); } while (0)
; #define PG8_LDB(dst, b, h) do { _Pragma("unroll") for (int n = 0; n < 2; ++n) _Pragma("unroll") for (int k = 0; k < 2; ++k) dst[n][k] = *(const PG8_LAS bf16x8*)(lds + PG8_SB(b, h) + boff + n * 2048 + k * 1024); } while (0)
; #define PG8_WAIT_V(n) asm volatile("s_waitcnt vmcnt(" #n ")" ::: "memory")
; #define PG8_WAIT_L(n) asm volatile("s_waitcnt lgkmcnt(" #n ")" ::: "memory")
; #define PG8_BAR __builtin_amdgcn_s_barrier()
; #define PG8_SCHED __builtin_amdgcn_sched_barrier(0)
; template <class Epi, class Sched, bool ALIGN_EPI, bool FP8 = false>
; __device__ __forceinline__ void gemm_phase(PG8_LAS unsigned char* lds, const Gemm g, const Sched& S, const Epi& E, const int wid, const int lane) {
;     ...
;         for (int t = 0; t < nt; t += 2) {
;             const bool last = (t == nt - 2);
;             const char* a1 = cA + (size_t)(t + 1) * kstep;
;             const char* a2 = last ? nA : cA + (size_t)(t + 2) * kstep; const char* b2 = last ? nB : cB + (size_t)(t + 2) * kstep;
;             const char* a3 = a2 + kstep; const char* b3 = b2 + kstep;
;             PG8_LDB(B0, 0, 0); PG8_LDB(B1, 0, 1); PG8_SCHED; PG8_LDA(At, 0, 0); PG8_STAGE(PG8_SA(1, 1), a1 + hstepA, vc1);
;             if (GA && last && has_next) { const u32x4 q = *gslot; vc0[0] = q.x; vc0[1] = q.y; vc1[0] = q.z; vc1[1] = q.w; }
;     ...
;             PG8_LDA(At, 1, 1); PG8_STAGE(PG8_SB(1, 0), b3, voffB); PG8_STAGE(PG8_SB(1, 1), b3 + hstep, voffB); PG8_STAGE(PG8_SA(1, 0), a3, vc0);
;             PG8_WAIT_V(8); PG8_WAIT_L(0); PG8_BAR; PG8_MMA(1, 0, At, B0); PG8_MMA(1, 1, At, B1); PG8_BAR; PG8_SCHED;
	ds_read_b128 v[32:35], v209 offset:49152
	ds_read_b128 v[36:39], v209 offset:50176
	ds_read_b128 v[40:43], v209 offset:51200
	ds_read_b128 v[44:47], v209 offset:52224
	ds_read_b128 v[48:51], v209 offset:53248
	ds_read_b128 v[52:55], v209 offset:54272
	ds_read_b128 v[56:59], v209 offset:55296
	ds_read_b128 v[60:63], v209 offset:56320
	s_mov_b32 m0, s69
	s_nop 0
	global_load_lds_dwordx4 v200, s[38:39]
	s_mov_b32 m0, s70
	s_nop 0
	global_load_lds_dwordx4 v202, s[38:39]
	s_add_u32 s38, s38, s16
	s_addc_u32 s39, s39, s17
	s_mov_b32 m0, s73
	s_nop 0
	global_load_lds_dwordx4 v200, s[38:39]
	s_mov_b32 m0, s74
	s_nop 0
	global_load_lds_dwordx4 v202, s[38:39]
	s_mov_b32 m0, s71
	s_nop 0
	global_load_lds_dwordx4 v64, s[8:9]
	s_mov_b32 m0, s72
	s_nop 0
	global_load_lds_dwordx4 v65, s[8:9]
	s_waitcnt vmcnt(8)
	s_waitcnt lgkmcnt(0)
	s_barrier
	s_setprio 1
	s_waitcnt lgkmcnt(6)
	v_mfma_scale_f32_16x16x128_f8f6f4 v[128:131], v[0:7], v[32:39], v[128:131], v210, v211 op_sel_hi:[0,0,0]
	v_mfma_scale_f32_16x16x128_f8f6f4 v[120:123], v[8:15], v[32:39], v[120:123], v210, v211 op_sel_hi:[0,0,0]
	s_waitcnt lgkmcnt(4)
	v_mfma_scale_f32_16x16x128_f8f6f4 v[112:115], v[0:7], v[40:47], v[112:115], v210, v211 op_sel_hi:[0,0,0]
	v_mfma_scale_f32_16x16x128_f8f6f4 v[104:107], v[8:15], v[40:47], v[104:107], v210, v211 op_sel_hi:[0,0,0]
	s_waitcnt lgkmcnt(2)
	v_mfma_scale_f32_16x16x128_f8f6f4 v[96:99], v[0:7], v[48:55], v[96:99], v210, v211 op_sel_hi:[0,0,0]
	v_mfma_scale_f32_16x16x128_f8f6f4 v[88:91], v[8:15], v[48:55], v[88:91], v210, v211 op_sel_hi:[0,0,0]
	s_waitcnt lgkmcnt(0)
	v_mfma_scale_f32_16x16x128_f8f6f4 v[80:83], v[0:7], v[56:63], v[80:83], v210, v211 op_sel_hi:[0,0,0]
	v_mfma_scale_f32_16x16x128_f8f6f4 v[72:75], v[8:15], v[56:63], v[72:75], v210, v211 op_sel_hi:[0,0,0]
	s_setprio 0
	s_setprio 1
	v_mfma_scale_f32_16x16x128_f8f6f4 v[124:127], v[16:23], v[32:39], v[124:127], v210, v211 op_sel_hi:[0,0,0]
	v_mfma_scale_f32_16x16x128_f8f6f4 v[116:119], v[24:31], v[32:39], v[116:119], v210, v211 op_sel_hi:[0,0,0]
	v_mfma_scale_f32_16x16x128_f8f6f4 v[108:111], v[16:23], v[40:47], v[108:111], v210, v211 op_sel_hi:[0,0,0]
	v_mfma_scale_f32_16x16x128_f8f6f4 v[100:103], v[24:31], v[40:47], v[100:103], v210, v211 op_sel_hi:[0,0,0]
	v_mfma_scale_f32_16x16x128_f8f6f4 v[92:95], v[16:23], v[48:55], v[92:95], v210, v211 op_sel_hi:[0,0,0]
	v_mfma_scale_f32_16x16x128_f8f6f4 v[84:87], v[24:31], v[48:55], v[84:87], v210, v211 op_sel_hi:[0,0,0]
	v_mfma_scale_f32_16x16x128_f8f6f4 v[76:79], v[16:23], v[56:63], v[76:79], v210, v211 op_sel_hi:[0,0,0]
	v_mfma_scale_f32_16x16x128_f8f6f4 v[68:71], v[24:31], v[56:63], v[68:71], v210, v211 op_sel_hi:[0,0,0]
	s_setprio 0
	s_barrier
	s_add_u32 s6, s6, 0x100
	s_addc_u32 s7, s7, 0
	s_cmp_ge_i32 s89, s68
	s_cbranch_scc1 .LBB0_1659
.LBB0_1638:
	ds_read_b128 v[24:27], v207
	ds_read_b128 v[28:31], v207 offset:1024
	ds_read_b128 v[16:19], v207 offset:2048
	ds_read_b128 v[20:23], v207 offset:3072
	ds_read_b128 v[8:11], v208
	ds_read_b128 v[12:15], v208 offset:1024
	ds_read_b128 v[0:3], v208 offset:2048
	ds_read_b128 v[4:7], v208 offset:3072
	s_cmp_eq_u32 s75, s89
	s_cselect_b64 s[38:39], -1, 0
	s_add_u32 s8, s20, s6
	s_addc_u32 s9, s21, s7
	s_add_u32 s8, s8, 0xffffff80
	s_addc_u32 s9, s9, -1
	ds_read_b128 v[56:59], v209
	ds_read_b128 v[60:63], v209 offset:1024
	ds_read_b128 v[48:51], v209 offset:2048
	ds_read_b128 v[52:55], v209 offset:3072
	ds_read_b128 v[40:43], v209 offset:4096
	ds_read_b128 v[44:47], v209 offset:5120
	ds_read_b128 v[32:35], v209 offset:6144
	ds_read_b128 v[36:39], v209 offset:7168
	s_mov_b32 m0, s82
	s_nop 0
	global_load_lds_dwordx4 v66, s[8:9]
	s_and_b64 s[40:41], s[36:37], s[38:39]
	s_mov_b32 m0, s83
	s_nop 0
	global_load_lds_dwordx4 v67, s[8:9]
	s_andn2_b64 vcc, exec, s[40:41]
	s_cbranch_vccnz .LBB0_1637
	v_lshl_add_u32 v64, v224, 11, v198
	v_lshl_add_u32 v65, v225, 11, v196
	v_lshl_add_u32 v66, v226, 11, v198
	v_lshl_add_u32 v67, v227, 11, v196
	s_branch .LBB0_1637

; template <class Epi, class Sched, bool ALIGN_EPI, bool FP8 = false>
; __device__ __forceinline__ void gemm_phase(PG8_LAS unsigned char* lds, const Gemm g, const Sched& S, const Epi& E, const int wid, const int lane) {
;     ...
;         if (GA && has_next) {
;             u32x4 q; q.x = S.tok_off(nxt, rA[0]) + cA2[0]; q.y = S.tok_off(nxt, rA[1]) + cA2[1]; q.z = S.tok_off(nxt, HALF + rA[0]) + cA2[0]; q.w = S.tok_off(nxt, HALF + rA[1]) + cA2[1];
;             *gslot = q;
;     __device__ __forceinline__ unsigned tok_off(const Unit& u, int r) const {
;         const int e = tileE[u.pm], local = (u.pm - tb[e]) * 256 + r;
;         int tok = local;
;         if (e < NE) tok = (local < cnt[e]) ? list[(size_t)e * LISTCAP + local] : 0;
;         return (unsigned)tok * K2;
;     }
.LBB0_1641:
	s_lshl_b32 s6, s85, 2
	s_add_i32 s6, s6, 0x20800
	v_mov_b32_e32 v0, s6
	ds_read_b32 v1, v0
	s_waitcnt lgkmcnt(0)
	s_nop 0
	v_readfirstlane_b32 s38, v1
	s_nop 3
	s_lshl_b32 s6, s38, 2
	s_add_i32 s7, s6, 0x21000
	s_add_i32 s6, s6, 0x21200
	v_mov_b32_e32 v0, s7
	v_mov_b32_e32 v1, s6
	ds_read_b32 v0, v0
	ds_read_b32 v1, v1
	s_waitcnt lgkmcnt(0)
	v_sub_u32_e32 v0, s85, v0
	v_lshlrev_b32_e32 v4, 8, v0
	v_or_b32_e32 v6, 0x80, v4
	v_add_u32_e32 v0, v4, v199
	v_add_u32_e32 v2, v4, v204
	v_add_u32_e32 v4, v6, v199
	v_add_u32_e32 v6, v6, v204
	v_mov_b32_e32 v224, v0
	v_mov_b32_e32 v225, v2
	v_mov_b32_e32 v226, v4
	v_mov_b32_e32 v227, v6
	s_cmp_gt_i32 s38, 63
	s_cbranch_scc1 .LBB0_1657
	s_ashr_i32 s39, s38, 31
	s_lshl_b64 s[40:41], s[38:39], 16
	s_add_u32 s40, s14, s40
	s_addc_u32 s41, s15, s41
	v_cmp_lt_i32_e32 vcc, v0, v1
	v_lshlrev_b32_e32 v220, 2, v0
	v_mov_b32_e32 v224, 0
	s_and_saveexec_b64 s[6:7], vcc
	s_cbranch_execz .Lp6b_g0
	global_load_dword v224, v220, s[40:41]
	s_add_i32 s100, s100, 1
